# v56 + gate/up K-loop: 12 of 16 LDS-DMA loads per iteration use SGPR base + 32-bit lane offset (saddr form), 12 v_lshl_add_u64 pointer builds removed
# speedup vs baseline: 1.0188x; 1.0066x over previous
; #define PG8_STAGE(bufoff, gbase, voff) do { _Pragma("unroll") for (int _i = 0; _i < 2; ++_i) \
;         __builtin_amdgcn_global_load_lds((const unsigned*)((const char*)(gbase) + (voff)[_i]), (PG8_LAS unsigned*)(lds + (bufoff) + ldsw + _i * 8192), 16, 0, 0); } while (0)
; #define PG8_LDA(dst, b, h) do { _Pragma("unroll") for (int m = 0; m < 4; ++m) _Pragma("unroll") for (int k = 0; k < 2; ++k) dst[m][k] = *(const PG8_LAS bf16x8*)(lds + PG8_SA(b, h) + aoff + m * 2048 + k * 1024); } while (0)
; #define PG8_LDB(dst, b, h) do { _Pragma("unroll") for (int n = 0; n < 2; ++n) _Pragma("unroll") for (int k = 0; k < 2; ++k) dst[n][k] = *(const PG8_LAS bf16x8*)(lds + PG8_SB(b, h) + boff + n * 2048 + k * 1024); } while (0)
; #define PG8_MMA(ai, bj, At, Bt) do { __builtin_amdgcn_s_setprio(1); _Pragma("unroll") for (int m = 0; m < 4; ++m) _Pragma("unroll") for (int n = 0; n < 2; ++n) _Pragma("unroll") for (int k = 0; k < 2; ++k) \
;         acc[ai][bj][m][n] = __builtin_amdgcn_mfma_f32_16x16x32_bf16(Bt[n][k], At[m][k], acc[ai][bj][m][n], 0, 0, 0); __builtin_amdgcn_s_setprio(0); } while (0)
; #define PG8_WAIT_V(n) asm volatile("s_waitcnt vmcnt(" #n ")" ::: "memory")
; #define PG8_WAIT_L(n) asm volatile("s_waitcnt lgkmcnt(" #n ")" ::: "memory")
; #define PG8_BAR __builtin_amdgcn_s_barrier()
; #define PG8_SCHED __builtin_amdgcn_sched_barrier(0)
; template <class Epi, class Sched, bool ALIGN_EPI = false, bool SP2 = false>
; __device__ __forceinline__ void gemm_phase(PG8_LAS unsigned char* lds, const Gemm g, const Sched& S, const Epi& E) {
;     ...
;             if (last && has_next) S.a_ready(nxt);
;             if constexpr (SP2) {
;             PG8_LDB(B0, 0, 0); PG8_LDB(B1, 0, 1); PG8_SCHED; PG8_LDA(At, 0, 0); PG8_STAGE(PG8_SA(1, 1), a1 + hstepA, voffA);
;             PG8_WAIT_V(8); PG8_WAIT_L(0); PG8_BAR; PG8_MMA(0, 0, At, B0); PG8_MMA(0, 1, At, B1); PG8_BAR; PG8_SCHED;
;             PG8_LDA(At, 0, 1); PG8_STAGE(PG8_SB(0, 0), b2, voffB); PG8_STAGE(PG8_SB(0, 1), b2 + hstepB, voffB); PG8_STAGE(PG8_SA(0, 0), a2, voffA);
.LBB0_152:
	s_ashr_i32 s15, s14, 31
	s_lshl_b64 s[16:17], s[14:15], 19
	s_add_u32 s16, s31, s16
	s_addc_u32 s17, s33, s17
	s_and_b64 s[18:19], s[2:3], exec
	s_cselect_b32 s15, s17, s25
	s_cselect_b32 s49, s16, s24
	s_ashr_i32 s13, s12, 31
	s_lshl_b64 s[18:19], s[12:13], 19
	s_add_u32 s18, s34, s18
	s_addc_u32 s19, s35, s19
	s_and_b64 s[26:27], s[2:3], exec
	s_cselect_b32 s13, s19, s23
	s_cselect_b32 s50, s18, s22
	s_add_u32 s51, s22, 0x100
	s_addc_u32 s52, s23, 0
	s_add_u32 s22, s24, 0x40080
	s_addc_u32 s23, s25, 0
	s_mov_b32 s53, -2
	s_add_u32 s24, s22, 0xfffc0080
	s_addc_u32 s25, s23, -1
	s_add_i32 s54, 0, 0x10000
	s_cmp_eq_u32 s53, 12
	s_cselect_b32 s27, s15, s25
	s_cselect_b32 s26, s49, s24
	v_add_u32_e32 v144, s54, v147
	s_cselect_b32 s25, s13, s52
	s_cselect_b32 s24, s50, s51
	s_add_i32 s56, 0, 0x14000
	ds_read_b128 v[150:153], v144
	ds_read_b128 v[154:157], v144 offset:1024
	ds_read_b128 v[158:161], v144 offset:2048
	ds_read_b128 v[162:165], v144 offset:3072
	v_add_u32_e32 v144, s56, v147
	ds_read_b128 v[166:169], v144
	ds_read_b128 v[170:173], v144 offset:1024
	ds_read_b128 v[174:177], v144 offset:2048
	ds_read_b128 v[178:181], v144 offset:3072
	s_add_i32 m0, s41, 0xc000
	ds_read_b128 v[182:185], v149
	ds_read_b128 v[186:189], v149 offset:1024
	ds_read_b128 v[190:193], v149 offset:2048
	ds_read_b128 v[194:197], v149 offset:3072
	ds_read_b128 v[210:213], v149 offset:4096
	ds_read_b128 v[226:229], v149 offset:5120
	ds_read_b128 v[230:233], v149 offset:6144
	ds_read_b128 v[234:237], v149 offset:7168
	v_lshl_add_u64 v[244:245], v[240:241], 0, s[64:65]
	s_mov_b32 m0, s45
	s_nop 0
	global_load_lds_dwordx4 v[244:245], off
	v_lshl_add_u64 v[244:245], v[242:243], 0, s[64:65]
	s_mov_b32 m0, s46
	s_nop 0
	global_load_lds_dwordx4 v[244:245], off
	s_add_i32 m0, s41, 0xc000
	s_nop 0
	global_load_lds_dwordx4 v142, s[22:23]
	s_add_i32 m0, s41, 0xe000
	s_nop 0
	global_load_lds_dwordx4 v140, s[22:23]
	s_waitcnt vmcnt(8)
	s_waitcnt lgkmcnt(0)
	s_barrier
	s_setprio 1
	s_waitcnt lgkmcnt(0)
	v_mfma_f32_16x16x32_bf16 v[128:131], v[150:153], v[182:185], 0
	v_mfma_f32_16x16x32_bf16 v[120:123], v[158:161], v[182:185], 0
	v_mfma_f32_16x16x32_bf16 v[112:115], v[150:153], v[190:193], 0
	v_mfma_f32_16x16x32_bf16 v[104:107], v[158:161], v[190:193], 0
	v_mfma_f32_16x16x32_bf16 v[96:99], v[150:153], v[210:213], 0
	v_mfma_f32_16x16x32_bf16 v[88:91], v[158:161], v[210:213], 0
	v_mfma_f32_16x16x32_bf16 v[80:83], v[150:153], v[230:233], 0
	v_mfma_f32_16x16x32_bf16 v[72:75], v[158:161], v[230:233], 0
	v_mfma_f32_16x16x32_bf16 v[128:131], v[154:157], v[186:189], v[128:131]
	v_mfma_f32_16x16x32_bf16 v[120:123], v[162:165], v[186:189], v[120:123]
	v_mfma_f32_16x16x32_bf16 v[112:115], v[154:157], v[194:197], v[112:115]
	v_mfma_f32_16x16x32_bf16 v[104:107], v[162:165], v[194:197], v[104:107]
	v_mfma_f32_16x16x32_bf16 v[96:99], v[154:157], v[226:229], v[96:99]
	v_mfma_f32_16x16x32_bf16 v[88:91], v[162:165], v[226:229], v[88:91]
	v_mfma_f32_16x16x32_bf16 v[80:83], v[154:157], v[234:237], v[80:83]
	v_mfma_f32_16x16x32_bf16 v[72:75], v[162:165], v[234:237], v[72:75]
	s_setprio 0
	s_setprio 1
	v_mfma_f32_16x16x32_bf16 v[124:127], v[166:169], v[182:185], 0
	v_mfma_f32_16x16x32_bf16 v[116:119], v[174:177], v[182:185], 0
	v_mfma_f32_16x16x32_bf16 v[108:111], v[166:169], v[190:193], 0
	v_mfma_f32_16x16x32_bf16 v[100:103], v[174:177], v[190:193], 0
	v_mfma_f32_16x16x32_bf16 v[92:95], v[166:169], v[210:213], 0
	v_mfma_f32_16x16x32_bf16 v[84:87], v[174:177], v[210:213], 0
	v_mfma_f32_16x16x32_bf16 v[76:79], v[166:169], v[230:233], 0
	v_mfma_f32_16x16x32_bf16 v[68:71], v[174:177], v[230:233], 0
	v_mfma_f32_16x16x32_bf16 v[124:127], v[170:173], v[186:189], v[124:127]
	v_mfma_f32_16x16x32_bf16 v[116:119], v[178:181], v[186:189], v[116:119]
	v_mfma_f32_16x16x32_bf16 v[108:111], v[170:173], v[194:197], v[108:111]
	v_mfma_f32_16x16x32_bf16 v[100:103], v[178:181], v[194:197], v[100:103]
	v_mfma_f32_16x16x32_bf16 v[92:95], v[170:173], v[226:229], v[92:95]
	v_mfma_f32_16x16x32_bf16 v[84:87], v[178:181], v[226:229], v[84:87]
	v_mfma_f32_16x16x32_bf16 v[76:79], v[170:173], v[234:237], v[76:79]
	v_mfma_f32_16x16x32_bf16 v[68:71], v[178:181], v[234:237], v[68:71]
	s_setprio 0
	s_barrier
	s_add_i32 s54, s54, s39
	s_mov_b32 m0, s54
	ds_read_b128 v[182:185], v149 offset:16384
	ds_read_b128 v[186:189], v149 offset:17408
	ds_read_b128 v[190:193], v149 offset:18432
	ds_read_b128 v[194:197], v149 offset:19456
	ds_read_b128 v[210:213], v149 offset:20480
	ds_read_b128 v[226:229], v149 offset:21504
	ds_read_b128 v[230:233], v149 offset:22528
	ds_read_b128 v[234:237], v149 offset:23552
	global_load_lds_dwordx4 v136, s[24:25]
	s_add_i32 m0, s54, 0x2000
	s_add_u32 s54, s24, 0x40000
	s_addc_u32 s55, s25, 0
	s_add_i32 s56, s56, s39
	global_load_lds_dwordx4 v132, s[24:25]
	s_mov_b32 m0, s56
	v_lshl_add_u64 v[242:243], s[26:27], 0, v[134:135]
	global_load_lds_dwordx4 v136, s[54:55]
	s_add_i32 m0, s56, 0x2000
	s_nop 0
	global_load_lds_dwordx4 v132, s[54:55]
	v_lshl_add_u64 v[240:241], s[26:27], 0, v[138:139]
	s_waitcnt vmcnt(6)
	s_waitcnt lgkmcnt(0)
	s_barrier
; #define PG8_STAGE(bufoff, gbase, voff) do { _Pragma("unroll") for (int _i = 0; _i < 2; ++_i) \
;         __builtin_amdgcn_global_load_lds((const unsigned*)((const char*)(gbase) + (voff)[_i]), (PG8_LAS unsigned*)(lds + (bufoff) + ldsw + _i * 8192), 16, 0, 0); } while (0)
; #define PG8_LDA(dst, b, h) do { _Pragma("unroll") for (int m = 0; m < 4; ++m) _Pragma("unroll") for (int k = 0; k < 2; ++k) dst[m][k] = *(const PG8_LAS bf16x8*)(lds + PG8_SA(b, h) + aoff + m * 2048 + k * 1024); } while (0)
; #define PG8_LDB(dst, b, h) do { _Pragma("unroll") for (int n = 0; n < 2; ++n) _Pragma("unroll") for (int k = 0; k < 2; ++k) dst[n][k] = *(const PG8_LAS bf16x8*)(lds + PG8_SB(b, h) + boff + n * 2048 + k * 1024); } while (0)
; #define PG8_MMA(ai, bj, At, Bt) do { __builtin_amdgcn_s_setprio(1); _Pragma("unroll") for (int m = 0; m < 4; ++m) _Pragma("unroll") for (int n = 0; n < 2; ++n) _Pragma("unroll") for (int k = 0; k < 2; ++k) \
;         acc[ai][bj][m][n] = __builtin_amdgcn_mfma_f32_16x16x32_bf16(Bt[n][k], At[m][k], acc[ai][bj][m][n], 0, 0, 0); __builtin_amdgcn_s_setprio(0); } while (0)
; #define PG8_WAIT_V(n) asm volatile("s_waitcnt vmcnt(" #n ")" ::: "memory")
; #define PG8_WAIT_L(n) asm volatile("s_waitcnt lgkmcnt(" #n ")" ::: "memory")
; #define PG8_BAR __builtin_amdgcn_s_barrier()
; #define PG8_SCHED __builtin_amdgcn_sched_barrier(0)
; template <class Epi, class Sched, bool ALIGN_EPI = false, bool SP2 = false>
; __device__ __forceinline__ void gemm_phase(PG8_LAS unsigned char* lds, const Gemm g, const Sched& S, const Epi& E) {
;     ...
;             PG8_LDA(At, 0, 1); PG8_STAGE(PG8_SB(0, 0), b2, voffB); PG8_STAGE(PG8_SB(0, 1), b2 + hstepB, voffB); PG8_STAGE(PG8_SA(0, 0), a2, voffA);
;             PG8_WAIT_V(8); PG8_WAIT_L(0); PG8_BAR; PG8_MMA(1, 0, At, B0); PG8_MMA(1, 1, At, B1); PG8_BAR; PG8_SCHED;
;             PG8_LDB(B0, 1, 0); PG8_LDB(B1, 1, 1); PG8_SCHED; PG8_LDA(At, 1, 0); PG8_STAGE(PG8_SA(0, 1), a2 + hstepA, voffA);
;             PG8_WAIT_V(8); PG8_WAIT_L(0); PG8_BAR; PG8_MMA(0, 0, At, B0); PG8_MMA(0, 1, At, B1); PG8_BAR; PG8_SCHED;
	s_setprio 1
	s_waitcnt lgkmcnt(0)
	v_mfma_f32_16x16x32_bf16 v[64:67], v[150:153], v[182:185], 0
	v_mfma_f32_16x16x32_bf16 v[56:59], v[158:161], v[182:185], 0
	v_mfma_f32_16x16x32_bf16 v[48:51], v[150:153], v[190:193], 0
	v_mfma_f32_16x16x32_bf16 v[40:43], v[158:161], v[190:193], 0
	v_mfma_f32_16x16x32_bf16 v[32:35], v[150:153], v[210:213], 0
	v_mfma_f32_16x16x32_bf16 v[24:27], v[158:161], v[210:213], 0
	v_mfma_f32_16x16x32_bf16 v[16:19], v[150:153], v[230:233], 0
	v_mfma_f32_16x16x32_bf16 v[8:11], v[158:161], v[230:233], 0
	v_mfma_f32_16x16x32_bf16 v[64:67], v[154:157], v[186:189], v[64:67]
	v_mfma_f32_16x16x32_bf16 v[56:59], v[162:165], v[186:189], v[56:59]
	v_mfma_f32_16x16x32_bf16 v[48:51], v[154:157], v[194:197], v[48:51]
	v_mfma_f32_16x16x32_bf16 v[40:43], v[162:165], v[194:197], v[40:43]
	v_mfma_f32_16x16x32_bf16 v[32:35], v[154:157], v[226:229], v[32:35]
	v_mfma_f32_16x16x32_bf16 v[24:27], v[162:165], v[226:229], v[24:27]
	v_mfma_f32_16x16x32_bf16 v[16:19], v[154:157], v[234:237], v[16:19]
	v_mfma_f32_16x16x32_bf16 v[8:11], v[162:165], v[234:237], v[8:11]
	s_setprio 0
	s_setprio 1
	v_mfma_f32_16x16x32_bf16 v[60:63], v[166:169], v[182:185], 0
	v_mfma_f32_16x16x32_bf16 v[52:55], v[174:177], v[182:185], 0
	v_mfma_f32_16x16x32_bf16 v[44:47], v[166:169], v[190:193], 0
	v_mfma_f32_16x16x32_bf16 v[36:39], v[174:177], v[190:193], 0
	v_mfma_f32_16x16x32_bf16 v[28:31], v[166:169], v[210:213], 0
	v_mfma_f32_16x16x32_bf16 v[20:23], v[174:177], v[210:213], 0
	v_mfma_f32_16x16x32_bf16 v[12:15], v[166:169], v[230:233], 0
	v_mfma_f32_16x16x32_bf16 v[4:7], v[174:177], v[230:233], 0
	v_mfma_f32_16x16x32_bf16 v[60:63], v[170:173], v[186:189], v[60:63]
	v_mfma_f32_16x16x32_bf16 v[52:55], v[178:181], v[186:189], v[52:55]
	v_mfma_f32_16x16x32_bf16 v[44:47], v[170:173], v[194:197], v[44:47]
	v_mfma_f32_16x16x32_bf16 v[36:39], v[178:181], v[194:197], v[36:39]
	v_mfma_f32_16x16x32_bf16 v[28:31], v[170:173], v[226:229], v[28:31]
	v_mfma_f32_16x16x32_bf16 v[20:23], v[178:181], v[226:229], v[20:23]
	v_mfma_f32_16x16x32_bf16 v[12:15], v[170:173], v[234:237], v[12:15]
	v_mfma_f32_16x16x32_bf16 v[4:7], v[178:181], v[234:237], v[4:7]
	s_setprio 0
	s_barrier
	s_add_i32 s54, 0, 0x18000
	s_add_i32 s55, 0, 0x1c000
	v_add_u32_e32 v162, s54, v147
	v_add_u32_e32 v178, s55, v147
	ds_read_b128 v[150:153], v162
	ds_read_b128 v[154:157], v162 offset:1024
	ds_read_b128 v[158:161], v162 offset:2048
	ds_read_b128 v[162:165], v162 offset:3072
	ds_read_b128 v[166:169], v178
	ds_read_b128 v[170:173], v178 offset:1024
	ds_read_b128 v[174:177], v178 offset:2048
	ds_read_b128 v[178:181], v178 offset:3072
	s_add_u32 s26, s26, 0x40000
	s_addc_u32 s27, s27, 0
	s_mov_b32 m0, s43
	ds_read_b128 v[182:185], v149 offset:32768
	ds_read_b128 v[186:189], v149 offset:33792
	ds_read_b128 v[190:193], v149 offset:34816
	ds_read_b128 v[194:197], v149 offset:35840
	ds_read_b128 v[210:213], v149 offset:36864
	ds_read_b128 v[226:229], v149 offset:37888
	ds_read_b128 v[230:233], v149 offset:38912
	ds_read_b128 v[234:237], v149 offset:39936
	s_mov_b32 m0, s41
	s_nop 0
	global_load_lds_dwordx4 v[240:241], off
	s_mov_b32 m0, s42
	s_nop 0
	global_load_lds_dwordx4 v[242:243], off
	s_mov_b32 m0, s43
	s_nop 0
	global_load_lds_dwordx4 v138, s[26:27]
	s_mov_b32 m0, s44
	s_nop 0
	global_load_lds_dwordx4 v134, s[26:27]
	s_waitcnt vmcnt(8)
	s_waitcnt lgkmcnt(0)
	s_barrier
	s_setprio 1
	s_waitcnt lgkmcnt(0)
	v_mfma_f32_16x16x32_bf16 v[128:131], v[150:153], v[182:185], v[128:131]
	v_mfma_f32_16x16x32_bf16 v[120:123], v[158:161], v[182:185], v[120:123]
	v_mfma_f32_16x16x32_bf16 v[112:115], v[150:153], v[190:193], v[112:115]
	v_mfma_f32_16x16x32_bf16 v[104:107], v[158:161], v[190:193], v[104:107]
	v_mfma_f32_16x16x32_bf16 v[96:99], v[150:153], v[210:213], v[96:99]
	v_mfma_f32_16x16x32_bf16 v[88:91], v[158:161], v[210:213], v[88:91]
	v_mfma_f32_16x16x32_bf16 v[80:83], v[150:153], v[230:233], v[80:83]
	v_mfma_f32_16x16x32_bf16 v[72:75], v[158:161], v[230:233], v[72:75]
	v_mfma_f32_16x16x32_bf16 v[128:131], v[154:157], v[186:189], v[128:131]
	v_mfma_f32_16x16x32_bf16 v[120:123], v[162:165], v[186:189], v[120:123]
	v_mfma_f32_16x16x32_bf16 v[112:115], v[154:157], v[194:197], v[112:115]
	v_mfma_f32_16x16x32_bf16 v[104:107], v[162:165], v[194:197], v[104:107]
	v_mfma_f32_16x16x32_bf16 v[96:99], v[154:157], v[226:229], v[96:99]
	v_mfma_f32_16x16x32_bf16 v[88:91], v[162:165], v[226:229], v[88:91]
	v_mfma_f32_16x16x32_bf16 v[80:83], v[154:157], v[234:237], v[80:83]
	v_mfma_f32_16x16x32_bf16 v[72:75], v[162:165], v[234:237], v[72:75]
	s_setprio 0
	s_setprio 1
	v_mfma_f32_16x16x32_bf16 v[124:127], v[166:169], v[182:185], v[124:127]
	v_mfma_f32_16x16x32_bf16 v[116:119], v[174:177], v[182:185], v[116:119]
	v_mfma_f32_16x16x32_bf16 v[108:111], v[166:169], v[190:193], v[108:111]
	v_mfma_f32_16x16x32_bf16 v[100:103], v[174:177], v[190:193], v[100:103]
	v_mfma_f32_16x16x32_bf16 v[92:95], v[166:169], v[210:213], v[92:95]
	v_mfma_f32_16x16x32_bf16 v[84:87], v[174:177], v[210:213], v[84:87]
	v_mfma_f32_16x16x32_bf16 v[76:79], v[166:169], v[230:233], v[76:79]
	v_mfma_f32_16x16x32_bf16 v[68:71], v[174:177], v[230:233], v[68:71]
	v_mfma_f32_16x16x32_bf16 v[124:127], v[170:173], v[186:189], v[124:127]
	v_mfma_f32_16x16x32_bf16 v[116:119], v[178:181], v[186:189], v[116:119]
	v_mfma_f32_16x16x32_bf16 v[108:111], v[170:173], v[194:197], v[108:111]
	v_mfma_f32_16x16x32_bf16 v[100:103], v[178:181], v[194:197], v[100:103]
	v_mfma_f32_16x16x32_bf16 v[92:95], v[170:173], v[226:229], v[92:95]
	v_mfma_f32_16x16x32_bf16 v[84:87], v[178:181], v[226:229], v[84:87]
	v_mfma_f32_16x16x32_bf16 v[76:79], v[170:173], v[234:237], v[76:79]
	v_mfma_f32_16x16x32_bf16 v[68:71], v[178:181], v[234:237], v[68:71]
	s_setprio 0
	s_barrier
; #define PG8_STAGE(bufoff, gbase, voff) do { _Pragma("unroll") for (int _i = 0; _i < 2; ++_i) \
;         __builtin_amdgcn_global_load_lds((const unsigned*)((const char*)(gbase) + (voff)[_i]), (PG8_LAS unsigned*)(lds + (bufoff) + ldsw + _i * 8192), 16, 0, 0); } while (0)
; #define PG8_LDA(dst, b, h) do { _Pragma("unroll") for (int m = 0; m < 4; ++m) _Pragma("unroll") for (int k = 0; k < 2; ++k) dst[m][k] = *(const PG8_LAS bf16x8*)(lds + PG8_SA(b, h) + aoff + m * 2048 + k * 1024); } while (0)
; #define PG8_LDB(dst, b, h) do { _Pragma("unroll") for (int n = 0; n < 2; ++n) _Pragma("unroll") for (int k = 0; k < 2; ++k) dst[n][k] = *(const PG8_LAS bf16x8*)(lds + PG8_SB(b, h) + boff + n * 2048 + k * 1024); } while (0)
; #define PG8_MMA(ai, bj, At, Bt) do { __builtin_amdgcn_s_setprio(1); _Pragma("unroll") for (int m = 0; m < 4; ++m) _Pragma("unroll") for (int n = 0; n < 2; ++n) _Pragma("unroll") for (int k = 0; k < 2; ++k) \
;         acc[ai][bj][m][n] = __builtin_amdgcn_mfma_f32_16x16x32_bf16(Bt[n][k], At[m][k], acc[ai][bj][m][n], 0, 0, 0); __builtin_amdgcn_s_setprio(0); } while (0)
; #define PG8_WAIT_V(n) asm volatile("s_waitcnt vmcnt(" #n ")" ::: "memory")
; #define PG8_WAIT_L(n) asm volatile("s_waitcnt lgkmcnt(" #n ")" ::: "memory")
; #define PG8_BAR __builtin_amdgcn_s_barrier()
; #define PG8_SCHED __builtin_amdgcn_sched_barrier(0)
; template <class Epi, class Sched, bool ALIGN_EPI = false, bool SP2 = false>
; __device__ __forceinline__ void gemm_phase(PG8_LAS unsigned char* lds, const Gemm g, const Sched& S, const Epi& E) {
;     ...
;             PG8_LDB(B0, 0, 0); PG8_LDB(B1, 0, 1); PG8_SCHED; PG8_LDA(At, 0, 0); PG8_STAGE(PG8_SA(1, 1), a1 + hstepA, voffA);
;             PG8_WAIT_V(8); PG8_WAIT_L(0); PG8_BAR; PG8_MMA(0, 0, At, B0); PG8_MMA(0, 1, At, B1); PG8_BAR; PG8_SCHED;
;     ...
;             PG8_WAIT_V(8); PG8_WAIT_L(0); PG8_BAR; PG8_MMA(0, 0, At, B0); PG8_MMA(0, 1, At, B1); PG8_BAR; PG8_SCHED;
;             PG8_LDA(At, 1, 1); PG8_STAGE(PG8_SB(1, 0), b3, voffB); PG8_STAGE(PG8_SB(1, 1), b3 + hstepB, voffB); PG8_STAGE(PG8_SA(1, 0), a3, voffA);
;             PG8_WAIT_V(8); PG8_WAIT_L(0); PG8_BAR; PG8_MMA(1, 0, At, B0); PG8_MMA(1, 1, At, B1); PG8_BAR; PG8_SCHED;
	s_add_i32 s26, s54, s39
	s_add_i32 m0, s26, 0xffffff80
	ds_read_b128 v[182:185], v149 offset:49152
	ds_read_b128 v[186:189], v149 offset:50176
	ds_read_b128 v[190:193], v149 offset:51200
	ds_read_b128 v[194:197], v149 offset:52224
	ds_read_b128 v[210:213], v149 offset:53248
	ds_read_b128 v[226:229], v149 offset:54272
	ds_read_b128 v[230:233], v149 offset:55296
	ds_read_b128 v[234:237], v149 offset:56320
	global_load_lds_dwordx4 v136, s[24:25] offset:128
	s_add_i32 m0, s26, 0x1f80
	s_add_i32 s26, s55, s39
	global_load_lds_dwordx4 v132, s[24:25] offset:128
	s_add_u32 s24, s24, 0x40080
	s_addc_u32 s25, s25, 0
	s_mov_b32 m0, s26
	s_nop 0
	global_load_lds_dwordx4 v136, s[24:25]
	s_add_i32 m0, s26, 0x2000
	s_nop 0
	global_load_lds_dwordx4 v132, s[24:25]
	s_waitcnt vmcnt(6)
	s_waitcnt lgkmcnt(0)
	s_barrier
	s_setprio 1
	s_waitcnt lgkmcnt(0)
	v_mfma_f32_16x16x32_bf16 v[64:67], v[150:153], v[182:185], v[64:67]
	v_mfma_f32_16x16x32_bf16 v[56:59], v[158:161], v[182:185], v[56:59]
	v_mfma_f32_16x16x32_bf16 v[48:51], v[150:153], v[190:193], v[48:51]
	v_mfma_f32_16x16x32_bf16 v[40:43], v[158:161], v[190:193], v[40:43]
	v_mfma_f32_16x16x32_bf16 v[32:35], v[150:153], v[210:213], v[32:35]
	v_mfma_f32_16x16x32_bf16 v[24:27], v[158:161], v[210:213], v[24:27]
	v_mfma_f32_16x16x32_bf16 v[16:19], v[150:153], v[230:233], v[16:19]
	v_mfma_f32_16x16x32_bf16 v[8:11], v[158:161], v[230:233], v[8:11]
	v_mfma_f32_16x16x32_bf16 v[64:67], v[154:157], v[186:189], v[64:67]
	v_mfma_f32_16x16x32_bf16 v[56:59], v[162:165], v[186:189], v[56:59]
	v_mfma_f32_16x16x32_bf16 v[48:51], v[154:157], v[194:197], v[48:51]
	v_mfma_f32_16x16x32_bf16 v[40:43], v[162:165], v[194:197], v[40:43]
	v_mfma_f32_16x16x32_bf16 v[32:35], v[154:157], v[226:229], v[32:35]
	v_mfma_f32_16x16x32_bf16 v[24:27], v[162:165], v[226:229], v[24:27]
	v_mfma_f32_16x16x32_bf16 v[16:19], v[154:157], v[234:237], v[16:19]
	v_mfma_f32_16x16x32_bf16 v[8:11], v[162:165], v[234:237], v[8:11]
	s_setprio 0
	s_setprio 1
	v_mfma_f32_16x16x32_bf16 v[60:63], v[166:169], v[182:185], v[60:63]
	v_mfma_f32_16x16x32_bf16 v[52:55], v[174:177], v[182:185], v[52:55]
	v_mfma_f32_16x16x32_bf16 v[44:47], v[166:169], v[190:193], v[44:47]
	v_mfma_f32_16x16x32_bf16 v[36:39], v[174:177], v[190:193], v[36:39]
	v_mfma_f32_16x16x32_bf16 v[28:31], v[166:169], v[210:213], v[28:31]
	v_mfma_f32_16x16x32_bf16 v[20:23], v[174:177], v[210:213], v[20:23]
	v_mfma_f32_16x16x32_bf16 v[12:15], v[166:169], v[230:233], v[12:15]
	v_mfma_f32_16x16x32_bf16 v[4:7], v[174:177], v[230:233], v[4:7]
	v_mfma_f32_16x16x32_bf16 v[60:63], v[170:173], v[186:189], v[60:63]
	v_mfma_f32_16x16x32_bf16 v[52:55], v[178:181], v[186:189], v[52:55]
	v_mfma_f32_16x16x32_bf16 v[44:47], v[170:173], v[194:197], v[44:47]
	v_mfma_f32_16x16x32_bf16 v[36:39], v[178:181], v[194:197], v[36:39]
	v_mfma_f32_16x16x32_bf16 v[28:31], v[170:173], v[226:229], v[28:31]
	v_mfma_f32_16x16x32_bf16 v[20:23], v[178:181], v[226:229], v[20:23]
	v_mfma_f32_16x16x32_bf16 v[12:15], v[170:173], v[234:237], v[12:15]
	v_mfma_f32_16x16x32_bf16 v[4:7], v[178:181], v[234:237], v[4:7]
	s_setprio 0
	s_barrier
	s_add_i32 s53, s53, 2
	s_add_u32 s51, s51, 0x100
	s_addc_u32 s52, s52, 0
	s_add_u32 s22, s22, 0x100
	s_addc_u32 s23, s23, 0
	s_cmp_gt_u32 s53, 13
	s_cbranch_scc1 .Lpeel_exit_0
.LBB0_153:
	s_add_u32 s24, s22, 0xfffc0080
	s_addc_u32 s25, s23, -1
	s_add_i32 s54, 0, 0x10000
	s_cmp_eq_u32 s53, 12
	s_cselect_b32 s27, s15, s25
	s_cselect_b32 s26, s49, s24
	v_add_u32_e32 v144, s54, v147
	s_cselect_b32 s25, s13, s52
	s_cselect_b32 s24, s50, s51
	s_add_i32 s56, 0, 0x14000
	ds_read_b128 v[150:153], v144
	ds_read_b128 v[154:157], v144 offset:1024
	ds_read_b128 v[158:161], v144 offset:2048
	ds_read_b128 v[162:165], v144 offset:3072
	v_add_u32_e32 v144, s56, v147
	ds_read_b128 v[166:169], v144
	ds_read_b128 v[170:173], v144 offset:1024
	ds_read_b128 v[174:177], v144 offset:2048
	ds_read_b128 v[178:181], v144 offset:3072
	s_add_i32 m0, s41, 0xc000
	ds_read_b128 v[182:185], v149
	ds_read_b128 v[186:189], v149 offset:1024
	ds_read_b128 v[190:193], v149 offset:2048
	ds_read_b128 v[194:197], v149 offset:3072
	ds_read_b128 v[210:213], v149 offset:4096
	ds_read_b128 v[226:229], v149 offset:5120
	ds_read_b128 v[230:233], v149 offset:6144
	ds_read_b128 v[234:237], v149 offset:7168
	v_lshl_add_u64 v[244:245], v[240:241], 0, s[64:65]
	s_mov_b32 m0, s45
	s_nop 0
	global_load_lds_dwordx4 v[244:245], off
	v_lshl_add_u64 v[244:245], v[242:243], 0, s[64:65]
	s_mov_b32 m0, s46
	s_nop 0
	global_load_lds_dwordx4 v[244:245], off
	s_add_i32 m0, s41, 0xc000
	s_nop 0
	global_load_lds_dwordx4 v142, s[22:23]
	s_add_i32 m0, s41, 0xe000
	s_nop 0
	global_load_lds_dwordx4 v140, s[22:23]
	s_waitcnt vmcnt(8)
	s_waitcnt lgkmcnt(0)
	s_barrier
; #define PG8_STAGE(bufoff, gbase, voff) do { _Pragma("unroll") for (int _i = 0; _i < 2; ++_i) \
;         __builtin_amdgcn_global_load_lds((const unsigned*)((const char*)(gbase) + (voff)[_i]), (PG8_LAS unsigned*)(lds + (bufoff) + ldsw + _i * 8192), 16, 0, 0); } while (0)
; #define PG8_LDA(dst, b, h) do { _Pragma("unroll") for (int m = 0; m < 4; ++m) _Pragma("unroll") for (int k = 0; k < 2; ++k) dst[m][k] = *(const PG8_LAS bf16x8*)(lds + PG8_SA(b, h) + aoff + m * 2048 + k * 1024); } while (0)
; #define PG8_LDB(dst, b, h) do { _Pragma("unroll") for (int n = 0; n < 2; ++n) _Pragma("unroll") for (int k = 0; k < 2; ++k) dst[n][k] = *(const PG8_LAS bf16x8*)(lds + PG8_SB(b, h) + boff + n * 2048 + k * 1024); } while (0)
; #define PG8_MMA(ai, bj, At, Bt) do { __builtin_amdgcn_s_setprio(1); _Pragma("unroll") for (int m = 0; m < 4; ++m) _Pragma("unroll") for (int n = 0; n < 2; ++n) _Pragma("unroll") for (int k = 0; k < 2; ++k) \
;         acc[ai][bj][m][n] = __builtin_amdgcn_mfma_f32_16x16x32_bf16(Bt[n][k], At[m][k], acc[ai][bj][m][n], 0, 0, 0); __builtin_amdgcn_s_setprio(0); } while (0)
; #define PG8_WAIT_V(n) asm volatile("s_waitcnt vmcnt(" #n ")" ::: "memory")
; #define PG8_WAIT_L(n) asm volatile("s_waitcnt lgkmcnt(" #n ")" ::: "memory")
; #define PG8_BAR __builtin_amdgcn_s_barrier()
; #define PG8_SCHED __builtin_amdgcn_sched_barrier(0)
; template <class Epi, class Sched, bool ALIGN_EPI = false, bool SP2 = false>
; __device__ __forceinline__ void gemm_phase(PG8_LAS unsigned char* lds, const Gemm g, const Sched& S, const Epi& E) {
;     ...
;             PG8_LDB(B0, 0, 0); PG8_LDB(B1, 0, 1); PG8_SCHED; PG8_LDA(At, 0, 0); PG8_STAGE(PG8_SA(1, 1), a1 + hstepA, voffA);
;             PG8_WAIT_V(8); PG8_WAIT_L(0); PG8_BAR; PG8_MMA(0, 0, At, B0); PG8_MMA(0, 1, At, B1); PG8_BAR; PG8_SCHED;
;             PG8_LDA(At, 0, 1); PG8_STAGE(PG8_SB(0, 0), b2, voffB); PG8_STAGE(PG8_SB(0, 1), b2 + hstepB, voffB); PG8_STAGE(PG8_SA(0, 0), a2, voffA);
;             PG8_WAIT_V(8); PG8_WAIT_L(0); PG8_BAR; PG8_MMA(1, 0, At, B0); PG8_MMA(1, 1, At, B1); PG8_BAR; PG8_SCHED;
	s_setprio 1
	s_waitcnt lgkmcnt(0)
	v_mfma_f32_16x16x32_bf16 v[128:131], v[150:153], v[182:185], v[128:131]
	v_mfma_f32_16x16x32_bf16 v[120:123], v[158:161], v[182:185], v[120:123]
	v_mfma_f32_16x16x32_bf16 v[112:115], v[150:153], v[190:193], v[112:115]
	v_mfma_f32_16x16x32_bf16 v[104:107], v[158:161], v[190:193], v[104:107]
	v_mfma_f32_16x16x32_bf16 v[96:99], v[150:153], v[210:213], v[96:99]
	v_mfma_f32_16x16x32_bf16 v[88:91], v[158:161], v[210:213], v[88:91]
	v_mfma_f32_16x16x32_bf16 v[80:83], v[150:153], v[230:233], v[80:83]
	v_mfma_f32_16x16x32_bf16 v[72:75], v[158:161], v[230:233], v[72:75]
	v_mfma_f32_16x16x32_bf16 v[128:131], v[154:157], v[186:189], v[128:131]
	v_mfma_f32_16x16x32_bf16 v[120:123], v[162:165], v[186:189], v[120:123]
	v_mfma_f32_16x16x32_bf16 v[112:115], v[154:157], v[194:197], v[112:115]
	v_mfma_f32_16x16x32_bf16 v[104:107], v[162:165], v[194:197], v[104:107]
	v_mfma_f32_16x16x32_bf16 v[96:99], v[154:157], v[226:229], v[96:99]
	v_mfma_f32_16x16x32_bf16 v[88:91], v[162:165], v[226:229], v[88:91]
	v_mfma_f32_16x16x32_bf16 v[80:83], v[154:157], v[234:237], v[80:83]
	v_mfma_f32_16x16x32_bf16 v[72:75], v[162:165], v[234:237], v[72:75]
	s_setprio 0
	s_setprio 1
	v_mfma_f32_16x16x32_bf16 v[124:127], v[166:169], v[182:185], v[124:127]
	v_mfma_f32_16x16x32_bf16 v[116:119], v[174:177], v[182:185], v[116:119]
	v_mfma_f32_16x16x32_bf16 v[108:111], v[166:169], v[190:193], v[108:111]
	v_mfma_f32_16x16x32_bf16 v[100:103], v[174:177], v[190:193], v[100:103]
	v_mfma_f32_16x16x32_bf16 v[92:95], v[166:169], v[210:213], v[92:95]
	v_mfma_f32_16x16x32_bf16 v[84:87], v[174:177], v[210:213], v[84:87]
	v_mfma_f32_16x16x32_bf16 v[76:79], v[166:169], v[230:233], v[76:79]
	v_mfma_f32_16x16x32_bf16 v[68:71], v[174:177], v[230:233], v[68:71]
	v_mfma_f32_16x16x32_bf16 v[124:127], v[170:173], v[186:189], v[124:127]
	v_mfma_f32_16x16x32_bf16 v[116:119], v[178:181], v[186:189], v[116:119]
	v_mfma_f32_16x16x32_bf16 v[108:111], v[170:173], v[194:197], v[108:111]
	v_mfma_f32_16x16x32_bf16 v[100:103], v[178:181], v[194:197], v[100:103]
	v_mfma_f32_16x16x32_bf16 v[92:95], v[170:173], v[226:229], v[92:95]
	v_mfma_f32_16x16x32_bf16 v[84:87], v[178:181], v[226:229], v[84:87]
	v_mfma_f32_16x16x32_bf16 v[76:79], v[170:173], v[234:237], v[76:79]
	v_mfma_f32_16x16x32_bf16 v[68:71], v[178:181], v[234:237], v[68:71]
	s_setprio 0
	s_barrier
	s_add_i32 s54, s54, s39
	s_mov_b32 m0, s54
	ds_read_b128 v[182:185], v149 offset:16384
	ds_read_b128 v[186:189], v149 offset:17408
	ds_read_b128 v[190:193], v149 offset:18432
	ds_read_b128 v[194:197], v149 offset:19456
	ds_read_b128 v[210:213], v149 offset:20480
	ds_read_b128 v[226:229], v149 offset:21504
	ds_read_b128 v[230:233], v149 offset:22528
	ds_read_b128 v[234:237], v149 offset:23552
	global_load_lds_dwordx4 v136, s[24:25]
	s_add_i32 m0, s54, 0x2000
	s_add_u32 s54, s24, 0x40000
	s_addc_u32 s55, s25, 0
	s_add_i32 s56, s56, s39
	global_load_lds_dwordx4 v132, s[24:25]
	s_mov_b32 m0, s56
	v_lshl_add_u64 v[242:243], s[26:27], 0, v[134:135]
	global_load_lds_dwordx4 v136, s[54:55]
	s_add_i32 m0, s56, 0x2000
	s_nop 0
	global_load_lds_dwordx4 v132, s[54:55]
	v_lshl_add_u64 v[240:241], s[26:27], 0, v[138:139]
	s_waitcnt vmcnt(6)
	s_waitcnt lgkmcnt(0)
	s_barrier
	s_setprio 1
	s_waitcnt lgkmcnt(0)
	v_mfma_f32_16x16x32_bf16 v[64:67], v[150:153], v[182:185], v[64:67]
	v_mfma_f32_16x16x32_bf16 v[56:59], v[158:161], v[182:185], v[56:59]
	v_mfma_f32_16x16x32_bf16 v[48:51], v[150:153], v[190:193], v[48:51]
	v_mfma_f32_16x16x32_bf16 v[40:43], v[158:161], v[190:193], v[40:43]
	v_mfma_f32_16x16x32_bf16 v[32:35], v[150:153], v[210:213], v[32:35]
	v_mfma_f32_16x16x32_bf16 v[24:27], v[158:161], v[210:213], v[24:27]
	v_mfma_f32_16x16x32_bf16 v[16:19], v[150:153], v[230:233], v[16:19]
	v_mfma_f32_16x16x32_bf16 v[8:11], v[158:161], v[230:233], v[8:11]
	v_mfma_f32_16x16x32_bf16 v[64:67], v[154:157], v[186:189], v[64:67]
	v_mfma_f32_16x16x32_bf16 v[56:59], v[162:165], v[186:189], v[56:59]
	v_mfma_f32_16x16x32_bf16 v[48:51], v[154:157], v[194:197], v[48:51]
	v_mfma_f32_16x16x32_bf16 v[40:43], v[162:165], v[194:197], v[40:43]
	v_mfma_f32_16x16x32_bf16 v[32:35], v[154:157], v[226:229], v[32:35]
	v_mfma_f32_16x16x32_bf16 v[24:27], v[162:165], v[226:229], v[24:27]
	v_mfma_f32_16x16x32_bf16 v[16:19], v[154:157], v[234:237], v[16:19]
	v_mfma_f32_16x16x32_bf16 v[8:11], v[162:165], v[234:237], v[8:11]
	s_setprio 0
	s_setprio 1
	v_mfma_f32_16x16x32_bf16 v[60:63], v[166:169], v[182:185], v[60:63]
	v_mfma_f32_16x16x32_bf16 v[52:55], v[174:177], v[182:185], v[52:55]
	v_mfma_f32_16x16x32_bf16 v[44:47], v[166:169], v[190:193], v[44:47]
	v_mfma_f32_16x16x32_bf16 v[36:39], v[174:177], v[190:193], v[36:39]
	v_mfma_f32_16x16x32_bf16 v[28:31], v[166:169], v[210:213], v[28:31]
	v_mfma_f32_16x16x32_bf16 v[20:23], v[174:177], v[210:213], v[20:23]
	v_mfma_f32_16x16x32_bf16 v[12:15], v[166:169], v[230:233], v[12:15]
	v_mfma_f32_16x16x32_bf16 v[4:7], v[174:177], v[230:233], v[4:7]
	v_mfma_f32_16x16x32_bf16 v[60:63], v[170:173], v[186:189], v[60:63]
	v_mfma_f32_16x16x32_bf16 v[52:55], v[178:181], v[186:189], v[52:55]
	v_mfma_f32_16x16x32_bf16 v[44:47], v[170:173], v[194:197], v[44:47]
	v_mfma_f32_16x16x32_bf16 v[36:39], v[178:181], v[194:197], v[36:39]
	v_mfma_f32_16x16x32_bf16 v[28:31], v[170:173], v[226:229], v[28:31]
	v_mfma_f32_16x16x32_bf16 v[20:23], v[178:181], v[226:229], v[20:23]
	v_mfma_f32_16x16x32_bf16 v[12:15], v[170:173], v[234:237], v[12:15]
	v_mfma_f32_16x16x32_bf16 v[4:7], v[178:181], v[234:237], v[4:7]
	s_setprio 0
	s_barrier
; #define PG8_STAGE(bufoff, gbase, voff) do { _Pragma("unroll") for (int _i = 0; _i < 2; ++_i) \
;         __builtin_amdgcn_global_load_lds((const unsigned*)((const char*)(gbase) + (voff)[_i]), (PG8_LAS unsigned*)(lds + (bufoff) + ldsw + _i * 8192), 16, 0, 0); } while (0)
; #define PG8_LDA(dst, b, h) do { _Pragma("unroll") for (int m = 0; m < 4; ++m) _Pragma("unroll") for (int k = 0; k < 2; ++k) dst[m][k] = *(const PG8_LAS bf16x8*)(lds + PG8_SA(b, h) + aoff + m * 2048 + k * 1024); } while (0)
; #define PG8_LDB(dst, b, h) do { _Pragma("unroll") for (int n = 0; n < 2; ++n) _Pragma("unroll") for (int k = 0; k < 2; ++k) dst[n][k] = *(const PG8_LAS bf16x8*)(lds + PG8_SB(b, h) + boff + n * 2048 + k * 1024); } while (0)
; #define PG8_MMA(ai, bj, At, Bt) do { __builtin_amdgcn_s_setprio(1); _Pragma("unroll") for (int m = 0; m < 4; ++m) _Pragma("unroll") for (int n = 0; n < 2; ++n) _Pragma("unroll") for (int k = 0; k < 2; ++k) \
;         acc[ai][bj][m][n] = __builtin_amdgcn_mfma_f32_16x16x32_bf16(Bt[n][k], At[m][k], acc[ai][bj][m][n], 0, 0, 0); __builtin_amdgcn_s_setprio(0); } while (0)
; #define PG8_WAIT_V(n) asm volatile("s_waitcnt vmcnt(" #n ")" ::: "memory")
; #define PG8_WAIT_L(n) asm volatile("s_waitcnt lgkmcnt(" #n ")" ::: "memory")
; #define PG8_BAR __builtin_amdgcn_s_barrier()
; #define PG8_SCHED __builtin_amdgcn_sched_barrier(0)
; template <class Epi, class Sched, bool ALIGN_EPI = false, bool SP2 = false>
; __device__ __forceinline__ void gemm_phase(PG8_LAS unsigned char* lds, const Gemm g, const Sched& S, const Epi& E) {
;     ...
;             PG8_LDB(B0, 1, 0); PG8_LDB(B1, 1, 1); PG8_SCHED; PG8_LDA(At, 1, 0); PG8_STAGE(PG8_SA(0, 1), a2 + hstepA, voffA);
;             PG8_WAIT_V(8); PG8_WAIT_L(0); PG8_BAR; PG8_MMA(0, 0, At, B0); PG8_MMA(0, 1, At, B1); PG8_BAR; PG8_SCHED;
;             PG8_LDA(At, 1, 1); PG8_STAGE(PG8_SB(1, 0), b3, voffB); PG8_STAGE(PG8_SB(1, 1), b3 + hstepB, voffB); PG8_STAGE(PG8_SA(1, 0), a3, voffA);
;             PG8_WAIT_V(8); PG8_WAIT_L(0); PG8_BAR; PG8_MMA(1, 0, At, B0); PG8_MMA(1, 1, At, B1); PG8_BAR; PG8_SCHED;
	s_add_i32 s54, 0, 0x18000
	s_add_i32 s55, 0, 0x1c000
	v_add_u32_e32 v162, s54, v147
	v_add_u32_e32 v178, s55, v147
	ds_read_b128 v[150:153], v162
	ds_read_b128 v[154:157], v162 offset:1024
	ds_read_b128 v[158:161], v162 offset:2048
	ds_read_b128 v[162:165], v162 offset:3072
	ds_read_b128 v[166:169], v178
	ds_read_b128 v[170:173], v178 offset:1024
	ds_read_b128 v[174:177], v178 offset:2048
	ds_read_b128 v[178:181], v178 offset:3072
	s_add_u32 s26, s26, 0x40000
	s_addc_u32 s27, s27, 0
	s_mov_b32 m0, s43
	ds_read_b128 v[182:185], v149 offset:32768
	ds_read_b128 v[186:189], v149 offset:33792
	ds_read_b128 v[190:193], v149 offset:34816
	ds_read_b128 v[194:197], v149 offset:35840
	ds_read_b128 v[210:213], v149 offset:36864
	ds_read_b128 v[226:229], v149 offset:37888
	ds_read_b128 v[230:233], v149 offset:38912
	ds_read_b128 v[234:237], v149 offset:39936
	s_mov_b32 m0, s41
	s_nop 0
	global_load_lds_dwordx4 v[240:241], off
	s_mov_b32 m0, s42
	s_nop 0
	global_load_lds_dwordx4 v[242:243], off
	s_mov_b32 m0, s43
	s_nop 0
	global_load_lds_dwordx4 v138, s[26:27]
	s_mov_b32 m0, s44
	s_nop 0
	global_load_lds_dwordx4 v134, s[26:27]
	s_waitcnt vmcnt(8)
	s_waitcnt lgkmcnt(0)
	s_barrier
	s_setprio 1
	s_waitcnt lgkmcnt(0)
	v_mfma_f32_16x16x32_bf16 v[128:131], v[150:153], v[182:185], v[128:131]
	v_mfma_f32_16x16x32_bf16 v[120:123], v[158:161], v[182:185], v[120:123]
	v_mfma_f32_16x16x32_bf16 v[112:115], v[150:153], v[190:193], v[112:115]
	v_mfma_f32_16x16x32_bf16 v[104:107], v[158:161], v[190:193], v[104:107]
	v_mfma_f32_16x16x32_bf16 v[96:99], v[150:153], v[210:213], v[96:99]
	v_mfma_f32_16x16x32_bf16 v[88:91], v[158:161], v[210:213], v[88:91]
	v_mfma_f32_16x16x32_bf16 v[80:83], v[150:153], v[230:233], v[80:83]
	v_mfma_f32_16x16x32_bf16 v[72:75], v[158:161], v[230:233], v[72:75]
	v_mfma_f32_16x16x32_bf16 v[128:131], v[154:157], v[186:189], v[128:131]
	v_mfma_f32_16x16x32_bf16 v[120:123], v[162:165], v[186:189], v[120:123]
	v_mfma_f32_16x16x32_bf16 v[112:115], v[154:157], v[194:197], v[112:115]
	v_mfma_f32_16x16x32_bf16 v[104:107], v[162:165], v[194:197], v[104:107]
	v_mfma_f32_16x16x32_bf16 v[96:99], v[154:157], v[226:229], v[96:99]
	v_mfma_f32_16x16x32_bf16 v[88:91], v[162:165], v[226:229], v[88:91]
	v_mfma_f32_16x16x32_bf16 v[80:83], v[154:157], v[234:237], v[80:83]
	v_mfma_f32_16x16x32_bf16 v[72:75], v[162:165], v[234:237], v[72:75]
	s_setprio 0
	s_setprio 1
	v_mfma_f32_16x16x32_bf16 v[124:127], v[166:169], v[182:185], v[124:127]
	v_mfma_f32_16x16x32_bf16 v[116:119], v[174:177], v[182:185], v[116:119]
	v_mfma_f32_16x16x32_bf16 v[108:111], v[166:169], v[190:193], v[108:111]
	v_mfma_f32_16x16x32_bf16 v[100:103], v[174:177], v[190:193], v[100:103]
	v_mfma_f32_16x16x32_bf16 v[92:95], v[166:169], v[210:213], v[92:95]
	v_mfma_f32_16x16x32_bf16 v[84:87], v[174:177], v[210:213], v[84:87]
	v_mfma_f32_16x16x32_bf16 v[76:79], v[166:169], v[230:233], v[76:79]
	v_mfma_f32_16x16x32_bf16 v[68:71], v[174:177], v[230:233], v[68:71]
	v_mfma_f32_16x16x32_bf16 v[124:127], v[170:173], v[186:189], v[124:127]
	v_mfma_f32_16x16x32_bf16 v[116:119], v[178:181], v[186:189], v[116:119]
	v_mfma_f32_16x16x32_bf16 v[108:111], v[170:173], v[194:197], v[108:111]
	v_mfma_f32_16x16x32_bf16 v[100:103], v[178:181], v[194:197], v[100:103]
	v_mfma_f32_16x16x32_bf16 v[92:95], v[170:173], v[226:229], v[92:95]
	v_mfma_f32_16x16x32_bf16 v[84:87], v[178:181], v[226:229], v[84:87]
	v_mfma_f32_16x16x32_bf16 v[76:79], v[170:173], v[234:237], v[76:79]
	v_mfma_f32_16x16x32_bf16 v[68:71], v[178:181], v[234:237], v[68:71]
	s_setprio 0
	s_barrier
	s_add_i32 s26, s54, s39
	s_add_i32 m0, s26, 0xffffff80
	ds_read_b128 v[182:185], v149 offset:49152
	ds_read_b128 v[186:189], v149 offset:50176
	ds_read_b128 v[190:193], v149 offset:51200
	ds_read_b128 v[194:197], v149 offset:52224
	ds_read_b128 v[210:213], v149 offset:53248
	ds_read_b128 v[226:229], v149 offset:54272
	ds_read_b128 v[230:233], v149 offset:55296
	ds_read_b128 v[234:237], v149 offset:56320
	global_load_lds_dwordx4 v136, s[24:25] offset:128
	s_add_i32 m0, s26, 0x1f80
	s_add_i32 s26, s55, s39
	global_load_lds_dwordx4 v132, s[24:25] offset:128
	s_add_u32 s24, s24, 0x40080
	s_addc_u32 s25, s25, 0
	s_mov_b32 m0, s26
	s_nop 0
	global_load_lds_dwordx4 v136, s[24:25]
	s_add_i32 m0, s26, 0x2000
	s_nop 0
	global_load_lds_dwordx4 v132, s[24:25]
	s_waitcnt vmcnt(6)
	s_waitcnt lgkmcnt(0)
	s_barrier
	s_setprio 1
	s_waitcnt lgkmcnt(0)
	v_mfma_f32_16x16x32_bf16 v[64:67], v[150:153], v[182:185], v[64:67]
	v_mfma_f32_16x16x32_bf16 v[56:59], v[158:161], v[182:185], v[56:59]
	v_mfma_f32_16x16x32_bf16 v[48:51], v[150:153], v[190:193], v[48:51]
	v_mfma_f32_16x16x32_bf16 v[40:43], v[158:161], v[190:193], v[40:43]
	v_mfma_f32_16x16x32_bf16 v[32:35], v[150:153], v[210:213], v[32:35]
	v_mfma_f32_16x16x32_bf16 v[24:27], v[158:161], v[210:213], v[24:27]
	v_mfma_f32_16x16x32_bf16 v[16:19], v[150:153], v[230:233], v[16:19]
	v_mfma_f32_16x16x32_bf16 v[8:11], v[158:161], v[230:233], v[8:11]
	v_mfma_f32_16x16x32_bf16 v[64:67], v[154:157], v[186:189], v[64:67]
	v_mfma_f32_16x16x32_bf16 v[56:59], v[162:165], v[186:189], v[56:59]
	v_mfma_f32_16x16x32_bf16 v[48:51], v[154:157], v[194:197], v[48:51]
	v_mfma_f32_16x16x32_bf16 v[40:43], v[162:165], v[194:197], v[40:43]
	v_mfma_f32_16x16x32_bf16 v[32:35], v[154:157], v[226:229], v[32:35]
	v_mfma_f32_16x16x32_bf16 v[24:27], v[162:165], v[226:229], v[24:27]
	v_mfma_f32_16x16x32_bf16 v[16:19], v[154:157], v[234:237], v[16:19]
	v_mfma_f32_16x16x32_bf16 v[8:11], v[162:165], v[234:237], v[8:11]
	s_setprio 0
	s_setprio 1
	v_mfma_f32_16x16x32_bf16 v[60:63], v[166:169], v[182:185], v[60:63]
	v_mfma_f32_16x16x32_bf16 v[52:55], v[174:177], v[182:185], v[52:55]
	v_mfma_f32_16x16x32_bf16 v[44:47], v[166:169], v[190:193], v[44:47]
	v_mfma_f32_16x16x32_bf16 v[36:39], v[174:177], v[190:193], v[36:39]
	v_mfma_f32_16x16x32_bf16 v[28:31], v[166:169], v[210:213], v[28:31]
	v_mfma_f32_16x16x32_bf16 v[20:23], v[174:177], v[210:213], v[20:23]
	v_mfma_f32_16x16x32_bf16 v[12:15], v[166:169], v[230:233], v[12:15]
	v_mfma_f32_16x16x32_bf16 v[4:7], v[174:177], v[230:233], v[4:7]
	v_mfma_f32_16x16x32_bf16 v[60:63], v[170:173], v[186:189], v[60:63]
	v_mfma_f32_16x16x32_bf16 v[52:55], v[178:181], v[186:189], v[52:55]
	v_mfma_f32_16x16x32_bf16 v[44:47], v[170:173], v[194:197], v[44:47]
	v_mfma_f32_16x16x32_bf16 v[36:39], v[178:181], v[194:197], v[36:39]
	v_mfma_f32_16x16x32_bf16 v[28:31], v[170:173], v[226:229], v[28:31]
	v_mfma_f32_16x16x32_bf16 v[20:23], v[178:181], v[226:229], v[20:23]
	v_mfma_f32_16x16x32_bf16 v[12:15], v[170:173], v[234:237], v[12:15]
	v_mfma_f32_16x16x32_bf16 v[4:7], v[178:181], v[234:237], v[4:7]
	s_setprio 0
	s_barrier
	s_add_i32 s53, s53, 2
	s_add_u32 s51, s51, 0x100
	s_addc_u32 s52, s52, 0
	s_add_u32 s22, s22, 0x100
	s_addc_u32 s23, s23, 0
	s_cmp_gt_u32 s53, 13
	s_cbranch_scc0 .LBB0_153
